# counted vmcnt across GEMM unit boundaries: per-unit full drains -> counted waits, first two waits of the peeled K-iteration relaxed by the 8 epilogue stores on non-first units
# baseline (speedup 1.0000x reference)
.LBB0_800:
	s_add_u32 s12, s20, 0x23000000
	s_addc_u32 s13, s21, 0
	s_add_u32 s14, s20, 0x23c00000
	s_addc_u32 s15, s21, 0
	s_add_u32 s16, s20, 0x24400000
	s_addc_u32 s17, s21, 0
	s_add_u32 s42, s20, 0x24500000
	s_addc_u32 s43, s21, 0
	s_add_u32 s44, s20, 0x25500000
	s_addc_u32 s45, s21, 0
	s_add_u32 s46, s20, 0x28500000
	s_addc_u32 s47, s21, 0
	s_add_u32 s48, s20, 0x200000
	s_addc_u32 s49, s21, 0
	s_add_u32 s50, s20, 0x300000
	s_addc_u32 s51, s21, 0
	s_add_u32 s76, s20, 0x700000
	s_addc_u32 s77, s21, 0
	s_add_i32 m0, s72, 0x18000
	v_lshl_add_u64 v[4:5], v[4:5], 0, s[24:25]
	s_waitcnt vmcnt(2)
	s_barrier
	global_load_lds_dwordx4 v[4:5], off
	v_lshl_add_u64 v[4:5], v[6:7], 0, s[24:25]
	s_add_i32 m0, s72, 0x1a000
	s_add_i32 s79, s72, 0x8000
	global_load_lds_dwordx4 v[4:5], off
	v_lshl_add_u64 v[4:5], v[12:13], 0, s[24:25]
	s_mov_b32 m0, s79
	s_add_i32 s80, s72, 0xa000
	global_load_lds_dwordx4 v[4:5], off
	v_lshl_add_u64 v[4:5], v[14:15], 0, s[24:25]
	s_mov_b32 m0, s80
	v_lshrrev_b32_e32 v23, 1, v21
	global_load_lds_dwordx4 v[4:5], off
	s_add_i32 m0, s72, 0x1c000
	v_lshl_add_u64 v[4:5], v[8:9], 0, s[24:25]
	global_load_lds_dwordx4 v[4:5], off
	v_lshl_add_u64 v[4:5], v[10:11], 0, s[24:25]
	s_add_i32 m0, s72, 0x1e000
	s_lshr_b32 s3, s3, 26
	global_load_lds_dwordx4 v[4:5], off
	v_and_b32_e32 v23, 24, v23
	v_and_b32_e32 v22, 15, v21
	s_add_i32 s3, s2, s3
	v_lshlrev_b32_e32 v24, 1, v23
	v_lshlrev_b32_e32 v21, 2, v21
	s_and_b32 s22, s22, 3
	s_ashr_i32 s78, s3, 6
	v_lshl_or_b32 v230, s83, 6, v22
	v_lshl_or_b32 v22, v22, 6, v24
	s_lshl_b32 s3, s83, 13
	v_and_b32_e32 v21, 32, v21
	v_bitop3_b32 v24, v22, s3, v21 bitop3:0xde
	s_lshl_b32 s3, s22, 12
	s_cmp_gt_i32 s2, 63
	s_cselect_b64 s[52:53], -1, 0
	s_add_i32 s81, s78, -2
	s_cmpk_lt_u32 s19, 0x100
	s_cselect_b64 s[54:55], -1, 0
	s_cmp_eq_u32 s22, 0
	s_cselect_b64 s[56:57], -1, 0
	s_addk_i32 s83, 0x200
	s_lshl_b32 s2, s22, 2
	v_add_u32_e32 v2, v20, v2
	s_add_u32 s2, s20, s2
	v_add_lshl_u32 v2, v2, v19, 1
	v_bitop3_b32 v231, v22, s3, v21 bitop3:0xde
	s_waitcnt vmcnt(6)
	s_addc_u32 s3, s21, 0
	v_lshl_add_u64 v[204:205], s[6:7], 0, v[2:3]
	v_add_u32_e32 v2, v18, v16
	s_add_u32 s58, s2, 0x400000
	v_add_lshl_u32 v2, v2, v17, 1
	s_mov_b32 s82, 0
	s_addc_u32 s59, s3, 0
	v_lshl_or_b32 v1, s22, 5, v23
	v_lshl_add_u64 v[206:207], s[6:7], 0, v[2:3]
	v_add_u32_e32 v240, 0, v24
	v_readlane_b32 s87, v254, 35
	v_readlane_b32 s84, v254, 48
	s_movk_i32 s88, 0xb9
	s_movk_i32 s89, 0x300
	v_readlane_b32 s90, v255, 10
	s_movk_i32 s91, 0xc00
	s_barrier
	s_mov_b32 s100, 0
	s_branch .LBB0_803

.LBB0_809:
	s_andn2_b64 vcc, exec, s[52:53]
	s_waitcnt vmcnt(8)
	s_cbranch_vccnz .LBB0_812
	s_add_u32 s26, s26, 0x80
	s_addc_u32 s27, s27, 0
	s_add_u32 s19, s30, 0x100
	s_addc_u32 s20, s31, 0
	s_mov_b32 s21, 0
	s_add_i32 s22, s21, 2
	s_add_u32 s23, s26, 0x80
	s_addc_u32 s28, s27, 0
	s_add_i32 s34, 0, 0x10000
	s_cmp_eq_u32 s81, s21
	s_cselect_b32 s31, s3, s28
	s_cselect_b32 s30, s2, s23
	v_add_u32_e32 v2, s34, v231
	s_cselect_b32 s29, s61, s20
	s_cselect_b32 s28, s60, s19
	s_add_i32 s21, 0, 0x14000
	ds_read_b128 v[100:103], v2
	ds_read_b128 v[104:107], v2 offset:1024
	ds_read_b128 v[108:111], v2 offset:2048
	ds_read_b128 v[112:115], v2 offset:3072
	v_add_u32_e32 v2, s21, v231
	ds_read_b128 v[132:135], v2
	ds_read_b128 v[136:139], v2 offset:1024
	ds_read_b128 v[140:143], v2 offset:2048
	ds_read_b128 v[144:147], v2 offset:3072
	v_lshl_add_u64 v[208:209], s[26:27], 0, v[204:205]
	s_add_i32 m0, s72, 0xc000
	ds_read_b128 v[164:167], v240
	ds_read_b128 v[168:171], v240 offset:1024
	ds_read_b128 v[172:175], v240 offset:2048
	ds_read_b128 v[176:179], v240 offset:3072
	ds_read_b128 v[180:183], v240 offset:4096
	ds_read_b128 v[184:187], v240 offset:5120
	ds_read_b128 v[188:191], v240 offset:6144
	ds_read_b128 v[192:195], v240 offset:7168
	global_load_lds_dwordx4 v[208:209], off
	v_lshl_add_u64 v[208:209], s[26:27], 0, v[206:207]
	s_add_i32 m0, s72, 0xe000
	s_nop 0
	global_load_lds_dwordx4 v[208:209], off
	s_cmp_eq_u32 s100, 0
	s_cbranch_scc1 .Lmy_w00a
	s_waitcnt vmcnt(16)
	s_branch .Lmy_w00b
.Lmy_w00a:
	s_waitcnt vmcnt(8)
.Lmy_w00b:
	s_waitcnt lgkmcnt(0)
	s_barrier
	s_setprio 1
	v_mfma_f32_16x16x32_bf16 v[160:163], v[100:103], v[164:167], 0
	v_mfma_f32_16x16x32_bf16 v[156:159], v[108:111], v[164:167], 0
	v_mfma_f32_16x16x32_bf16 v[128:131], v[100:103], v[172:175], 0
	v_mfma_f32_16x16x32_bf16 v[124:127], v[108:111], v[172:175], 0
	v_mfma_f32_16x16x32_bf16 v[96:99], v[100:103], v[180:183], 0
	v_mfma_f32_16x16x32_bf16 v[92:95], v[108:111], v[180:183], 0
	v_mfma_f32_16x16x32_bf16 v[80:83], v[100:103], v[188:191], 0
	v_mfma_f32_16x16x32_bf16 v[76:79], v[108:111], v[188:191], 0
	v_mfma_f32_16x16x32_bf16 v[160:163], v[104:107], v[168:171], v[160:163]
	v_mfma_f32_16x16x32_bf16 v[156:159], v[112:115], v[168:171], v[156:159]
	v_mfma_f32_16x16x32_bf16 v[128:131], v[104:107], v[176:179], v[128:131]
	v_mfma_f32_16x16x32_bf16 v[124:127], v[112:115], v[176:179], v[124:127]
	v_mfma_f32_16x16x32_bf16 v[96:99], v[104:107], v[184:187], v[96:99]
	v_mfma_f32_16x16x32_bf16 v[92:95], v[112:115], v[184:187], v[92:95]
	v_mfma_f32_16x16x32_bf16 v[80:83], v[104:107], v[192:195], v[80:83]
	v_mfma_f32_16x16x32_bf16 v[76:79], v[112:115], v[192:195], v[76:79]
	s_setprio 0
	s_setprio 1
	v_mfma_f32_16x16x32_bf16 v[152:155], v[132:135], v[164:167], 0
	v_mfma_f32_16x16x32_bf16 v[148:151], v[140:143], v[164:167], 0
	v_mfma_f32_16x16x32_bf16 v[120:123], v[132:135], v[172:175], 0
	v_mfma_f32_16x16x32_bf16 v[116:119], v[140:143], v[172:175], 0
	v_mfma_f32_16x16x32_bf16 v[88:91], v[132:135], v[180:183], 0
	v_mfma_f32_16x16x32_bf16 v[84:87], v[140:143], v[180:183], 0
	v_mfma_f32_16x16x32_bf16 v[72:75], v[132:135], v[188:191], 0
	v_mfma_f32_16x16x32_bf16 v[68:71], v[140:143], v[188:191], 0
	v_mfma_f32_16x16x32_bf16 v[152:155], v[136:139], v[168:171], v[152:155]
	v_mfma_f32_16x16x32_bf16 v[148:151], v[144:147], v[168:171], v[148:151]
	v_mfma_f32_16x16x32_bf16 v[120:123], v[136:139], v[176:179], v[120:123]
	v_mfma_f32_16x16x32_bf16 v[116:119], v[144:147], v[176:179], v[116:119]
	v_mfma_f32_16x16x32_bf16 v[88:91], v[136:139], v[184:187], v[88:91]
	v_mfma_f32_16x16x32_bf16 v[84:87], v[144:147], v[184:187], v[84:87]
	v_mfma_f32_16x16x32_bf16 v[72:75], v[136:139], v[192:195], v[72:75]
	v_mfma_f32_16x16x32_bf16 v[68:71], v[144:147], v[192:195], v[68:71]
	s_barrier
	s_setprio 0
	s_add_i32 s23, s34, s69
	v_lshl_add_u64 v[208:209], s[28:29], 0, v[200:201]
	s_mov_b32 m0, s23
	ds_read_b128 v[164:167], v240 offset:16384
	ds_read_b128 v[168:171], v240 offset:17408
	ds_read_b128 v[172:175], v240 offset:18432
	ds_read_b128 v[176:179], v240 offset:19456
	ds_read_b128 v[180:183], v240 offset:20480
	ds_read_b128 v[184:187], v240 offset:21504
	ds_read_b128 v[188:191], v240 offset:22528
	ds_read_b128 v[192:195], v240 offset:23552
	global_load_lds_dwordx4 v[208:209], off
	s_add_i32 m0, s23, 0x2000
	v_lshl_add_u64 v[210:211], s[28:29], 0, v[196:197]
	s_add_u32 s28, s28, s6
	s_addc_u32 s29, s29, s7
	s_add_i32 s21, s21, s69
	global_load_lds_dwordx4 v[210:211], off
	v_lshl_add_u64 v[218:219], s[28:29], 0, v[200:201]
	s_mov_b32 m0, s21
	v_lshl_add_u64 v[220:221], s[28:29], 0, v[196:197]
	global_load_lds_dwordx4 v[218:219], off
	s_add_i32 m0, s21, 0x2000
	v_lshl_add_u64 v[222:223], s[30:31], 0, v[202:203]
	global_load_lds_dwordx4 v[220:221], off
	s_mov_b32 m0, s72
	v_lshl_add_u64 v[224:225], s[30:31], 0, v[198:199]
	global_load_lds_dwordx4 v[222:223], off
	s_mov_b32 m0, s73
	s_nop 0
	global_load_lds_dwordx4 v[224:225], off
	s_cmp_eq_u32 s100, 0
	s_cbranch_scc1 .Lmy_w01a
	s_waitcnt vmcnt(16)
	s_branch .Lmy_w01b

.Lmy_w01b:
	s_mov_b32 s100, 1
	s_waitcnt lgkmcnt(0)
	s_barrier
	s_setprio 1
	v_mfma_f32_16x16x32_bf16 v[64:67], v[100:103], v[164:167], 0
	v_mfma_f32_16x16x32_bf16 v[60:63], v[108:111], v[164:167], 0
	v_mfma_f32_16x16x32_bf16 v[48:51], v[100:103], v[172:175], 0
	v_mfma_f32_16x16x32_bf16 v[44:47], v[108:111], v[172:175], 0
	v_mfma_f32_16x16x32_bf16 v[32:35], v[100:103], v[180:183], 0
	v_mfma_f32_16x16x32_bf16 v[28:31], v[108:111], v[180:183], 0
	v_mfma_f32_16x16x32_bf16 v[16:19], v[100:103], v[188:191], 0
	v_mfma_f32_16x16x32_bf16 v[12:15], v[108:111], v[188:191], 0
	v_mfma_f32_16x16x32_bf16 v[64:67], v[104:107], v[168:171], v[64:67]
	v_mfma_f32_16x16x32_bf16 v[60:63], v[112:115], v[168:171], v[60:63]
	v_mfma_f32_16x16x32_bf16 v[48:51], v[104:107], v[176:179], v[48:51]
	v_mfma_f32_16x16x32_bf16 v[44:47], v[112:115], v[176:179], v[44:47]
	v_mfma_f32_16x16x32_bf16 v[32:35], v[104:107], v[184:187], v[32:35]
	v_mfma_f32_16x16x32_bf16 v[28:31], v[112:115], v[184:187], v[28:31]
	v_mfma_f32_16x16x32_bf16 v[16:19], v[104:107], v[192:195], v[16:19]
	v_mfma_f32_16x16x32_bf16 v[12:15], v[112:115], v[192:195], v[12:15]
	s_setprio 0
	s_setprio 1
	v_mfma_f32_16x16x32_bf16 v[56:59], v[132:135], v[164:167], 0
	v_mfma_f32_16x16x32_bf16 v[52:55], v[140:143], v[164:167], 0
	v_mfma_f32_16x16x32_bf16 v[40:43], v[132:135], v[172:175], 0
	v_mfma_f32_16x16x32_bf16 v[36:39], v[140:143], v[172:175], 0
	v_mfma_f32_16x16x32_bf16 v[24:27], v[132:135], v[180:183], 0
	v_mfma_f32_16x16x32_bf16 v[20:23], v[140:143], v[180:183], 0
	v_mfma_f32_16x16x32_bf16 v[8:11], v[132:135], v[188:191], 0
	v_mfma_f32_16x16x32_bf16 v[4:7], v[140:143], v[188:191], 0
	v_mfma_f32_16x16x32_bf16 v[56:59], v[136:139], v[168:171], v[56:59]
	v_mfma_f32_16x16x32_bf16 v[52:55], v[144:147], v[168:171], v[52:55]
	v_mfma_f32_16x16x32_bf16 v[40:43], v[136:139], v[176:179], v[40:43]
	v_mfma_f32_16x16x32_bf16 v[36:39], v[144:147], v[176:179], v[36:39]
	v_mfma_f32_16x16x32_bf16 v[24:27], v[136:139], v[184:187], v[24:27]
	v_mfma_f32_16x16x32_bf16 v[20:23], v[144:147], v[184:187], v[20:23]
	v_mfma_f32_16x16x32_bf16 v[8:11], v[136:139], v[192:195], v[8:11]
	v_mfma_f32_16x16x32_bf16 v[4:7], v[144:147], v[192:195], v[4:7]
	s_barrier
	s_setprio 0
	s_add_i32 s21, 0, 0x18000
	v_add_u32_e32 v2, s21, v231
	s_add_i32 s23, 0, 0x1c000
	ds_read_b128 v[100:103], v2
	ds_read_b128 v[104:107], v2 offset:1024
	ds_read_b128 v[108:111], v2 offset:2048
	ds_read_b128 v[112:115], v2 offset:3072
	v_add_u32_e32 v2, s23, v231
	ds_read_b128 v[132:135], v2
	ds_read_b128 v[136:139], v2 offset:1024
	ds_read_b128 v[140:143], v2 offset:2048
	ds_read_b128 v[144:147], v2 offset:3072
	s_add_u32 s28, s30, s6
	s_addc_u32 s29, s31, s7
	s_mov_b32 m0, s74
	v_lshl_add_u64 v[226:227], s[28:29], 0, v[202:203]
	ds_read_b128 v[164:167], v240 offset:32768
	ds_read_b128 v[168:171], v240 offset:33792
	ds_read_b128 v[172:175], v240 offset:34816
	ds_read_b128 v[176:179], v240 offset:35840
	ds_read_b128 v[180:183], v240 offset:36864
	ds_read_b128 v[184:187], v240 offset:37888
	ds_read_b128 v[188:191], v240 offset:38912
	ds_read_b128 v[192:195], v240 offset:39936
	global_load_lds_dwordx4 v[226:227], off
	v_lshl_add_u64 v[226:227], s[28:29], 0, v[198:199]
	s_mov_b32 m0, s75
	s_nop 0
	global_load_lds_dwordx4 v[226:227], off
	s_waitcnt vmcnt(8)
	s_waitcnt lgkmcnt(0)
	s_barrier
	s_setprio 1
	v_mfma_f32_16x16x32_bf16 v[160:163], v[100:103], v[164:167], v[160:163]
	v_mfma_f32_16x16x32_bf16 v[156:159], v[108:111], v[164:167], v[156:159]
	v_mfma_f32_16x16x32_bf16 v[128:131], v[100:103], v[172:175], v[128:131]
	v_mfma_f32_16x16x32_bf16 v[124:127], v[108:111], v[172:175], v[124:127]
	v_mfma_f32_16x16x32_bf16 v[96:99], v[100:103], v[180:183], v[96:99]
	v_mfma_f32_16x16x32_bf16 v[92:95], v[108:111], v[180:183], v[92:95]
	v_mfma_f32_16x16x32_bf16 v[80:83], v[100:103], v[188:191], v[80:83]
	v_mfma_f32_16x16x32_bf16 v[76:79], v[108:111], v[188:191], v[76:79]
	v_mfma_f32_16x16x32_bf16 v[160:163], v[104:107], v[168:171], v[160:163]
	v_mfma_f32_16x16x32_bf16 v[156:159], v[112:115], v[168:171], v[156:159]
	v_mfma_f32_16x16x32_bf16 v[128:131], v[104:107], v[176:179], v[128:131]
	v_mfma_f32_16x16x32_bf16 v[124:127], v[112:115], v[176:179], v[124:127]
	v_mfma_f32_16x16x32_bf16 v[96:99], v[104:107], v[184:187], v[96:99]
	v_mfma_f32_16x16x32_bf16 v[92:95], v[112:115], v[184:187], v[92:95]
	v_mfma_f32_16x16x32_bf16 v[80:83], v[104:107], v[192:195], v[80:83]
	v_mfma_f32_16x16x32_bf16 v[76:79], v[112:115], v[192:195], v[76:79]
	s_setprio 0
	s_setprio 1
	v_mfma_f32_16x16x32_bf16 v[152:155], v[132:135], v[164:167], v[152:155]
	v_mfma_f32_16x16x32_bf16 v[148:151], v[140:143], v[164:167], v[148:151]
	v_mfma_f32_16x16x32_bf16 v[120:123], v[132:135], v[172:175], v[120:123]
	v_mfma_f32_16x16x32_bf16 v[116:119], v[140:143], v[172:175], v[116:119]
	v_mfma_f32_16x16x32_bf16 v[88:91], v[132:135], v[180:183], v[88:91]
	v_mfma_f32_16x16x32_bf16 v[84:87], v[140:143], v[180:183], v[84:87]
	v_mfma_f32_16x16x32_bf16 v[72:75], v[132:135], v[188:191], v[72:75]
	v_mfma_f32_16x16x32_bf16 v[68:71], v[140:143], v[188:191], v[68:71]
	v_mfma_f32_16x16x32_bf16 v[152:155], v[136:139], v[168:171], v[152:155]
	v_mfma_f32_16x16x32_bf16 v[148:151], v[144:147], v[168:171], v[148:151]
	v_mfma_f32_16x16x32_bf16 v[120:123], v[136:139], v[176:179], v[120:123]
	v_mfma_f32_16x16x32_bf16 v[116:119], v[144:147], v[176:179], v[116:119]
	v_mfma_f32_16x16x32_bf16 v[88:91], v[136:139], v[184:187], v[88:91]
	v_mfma_f32_16x16x32_bf16 v[84:87], v[144:147], v[184:187], v[84:87]
	v_mfma_f32_16x16x32_bf16 v[72:75], v[136:139], v[192:195], v[72:75]
	v_mfma_f32_16x16x32_bf16 v[68:71], v[144:147], v[192:195], v[68:71]
	s_barrier
	s_setprio 0
	s_add_i32 s21, s21, s69
	v_lshl_add_u64 v[208:209], v[208:209], 0, s[24:25]
	s_mov_b32 m0, s21
	ds_read_b128 v[164:167], v240 offset:49152
	ds_read_b128 v[168:171], v240 offset:50176
	ds_read_b128 v[172:175], v240 offset:51200
	ds_read_b128 v[176:179], v240 offset:52224
	ds_read_b128 v[180:183], v240 offset:53248
	ds_read_b128 v[184:187], v240 offset:54272
	ds_read_b128 v[188:191], v240 offset:55296
	ds_read_b128 v[192:195], v240 offset:56320
	global_load_lds_dwordx4 v[208:209], off
	v_lshl_add_u64 v[208:209], v[210:211], 0, s[24:25]
	s_add_i32 m0, s21, 0x2000
	s_add_i32 s21, s23, s69
	global_load_lds_dwordx4 v[208:209], off
	v_lshl_add_u64 v[208:209], v[218:219], 0, s[24:25]
	s_mov_b32 m0, s21
	s_nop 0
	global_load_lds_dwordx4 v[208:209], off
	v_lshl_add_u64 v[208:209], v[220:221], 0, s[24:25]
	s_add_i32 m0, s21, 0x2000
	s_nop 0
	global_load_lds_dwordx4 v[208:209], off
	v_lshl_add_u64 v[208:209], v[222:223], 0, s[24:25]
	s_mov_b32 m0, s79
	s_nop 0
	global_load_lds_dwordx4 v[208:209], off
	v_lshl_add_u64 v[208:209], v[224:225], 0, s[24:25]
	s_mov_b32 m0, s80
	s_nop 0
	global_load_lds_dwordx4 v[208:209], off
	s_waitcnt vmcnt(8)
	s_waitcnt lgkmcnt(0)
	s_barrier
	s_setprio 1
	v_mfma_f32_16x16x32_bf16 v[64:67], v[100:103], v[164:167], v[64:67]
	v_mfma_f32_16x16x32_bf16 v[60:63], v[108:111], v[164:167], v[60:63]
	v_mfma_f32_16x16x32_bf16 v[48:51], v[100:103], v[172:175], v[48:51]
	v_mfma_f32_16x16x32_bf16 v[44:47], v[108:111], v[172:175], v[44:47]
	v_mfma_f32_16x16x32_bf16 v[32:35], v[100:103], v[180:183], v[32:35]
	v_mfma_f32_16x16x32_bf16 v[28:31], v[108:111], v[180:183], v[28:31]
	v_mfma_f32_16x16x32_bf16 v[16:19], v[100:103], v[188:191], v[16:19]
	v_mfma_f32_16x16x32_bf16 v[12:15], v[108:111], v[188:191], v[12:15]
	v_mfma_f32_16x16x32_bf16 v[64:67], v[104:107], v[168:171], v[64:67]
	v_mfma_f32_16x16x32_bf16 v[60:63], v[112:115], v[168:171], v[60:63]
	v_mfma_f32_16x16x32_bf16 v[48:51], v[104:107], v[176:179], v[48:51]
	v_mfma_f32_16x16x32_bf16 v[44:47], v[112:115], v[176:179], v[44:47]
	v_mfma_f32_16x16x32_bf16 v[32:35], v[104:107], v[184:187], v[32:35]
	v_mfma_f32_16x16x32_bf16 v[28:31], v[112:115], v[184:187], v[28:31]
	v_mfma_f32_16x16x32_bf16 v[16:19], v[104:107], v[192:195], v[16:19]
	v_mfma_f32_16x16x32_bf16 v[12:15], v[112:115], v[192:195], v[12:15]
	s_setprio 0
	s_setprio 1
	v_mfma_f32_16x16x32_bf16 v[56:59], v[132:135], v[164:167], v[56:59]
	v_mfma_f32_16x16x32_bf16 v[52:55], v[140:143], v[164:167], v[52:55]
	v_mfma_f32_16x16x32_bf16 v[40:43], v[132:135], v[172:175], v[40:43]
	v_mfma_f32_16x16x32_bf16 v[36:39], v[140:143], v[172:175], v[36:39]
	v_mfma_f32_16x16x32_bf16 v[24:27], v[132:135], v[180:183], v[24:27]
	v_mfma_f32_16x16x32_bf16 v[20:23], v[140:143], v[180:183], v[20:23]
	v_mfma_f32_16x16x32_bf16 v[8:11], v[132:135], v[188:191], v[8:11]
	v_mfma_f32_16x16x32_bf16 v[4:7], v[140:143], v[188:191], v[4:7]
	v_mfma_f32_16x16x32_bf16 v[56:59], v[136:139], v[168:171], v[56:59]
	v_mfma_f32_16x16x32_bf16 v[52:55], v[144:147], v[168:171], v[52:55]
	v_mfma_f32_16x16x32_bf16 v[40:43], v[136:139], v[176:179], v[40:43]
	v_mfma_f32_16x16x32_bf16 v[36:39], v[144:147], v[176:179], v[36:39]
	v_mfma_f32_16x16x32_bf16 v[24:27], v[136:139], v[184:187], v[24:27]
	v_mfma_f32_16x16x32_bf16 v[20:23], v[144:147], v[184:187], v[20:23]
	v_mfma_f32_16x16x32_bf16 v[8:11], v[136:139], v[192:195], v[8:11]
	v_mfma_f32_16x16x32_bf16 v[4:7], v[144:147], v[192:195], v[4:7]
	s_barrier
	s_setprio 0
	s_add_u32 s26, s26, 0x100
	s_addc_u32 s27, s27, 0
	s_add_u32 s19, s19, 0x100
	s_addc_u32 s20, s20, 0
	s_cmp_ge_i32 s22, s78
	s_mov_b32 s21, s22
	s_cbranch_scc1 .LBB0_812

.LBB0_860:
	s_waitcnt vmcnt(4) lgkmcnt(0)
	v_add_u32_e32 v138, 0x80, v220
	s_and_b64 vcc, exec, s[40:41]
	s_mov_b64 s[26:27], -1
	s_cbranch_vccnz .LBB0_864
	v_mov_b32_e32 v119, 0
	v_mov_b32_e32 v118, 0
	v_mov_b32_e32 v117, 0
	v_mov_b32_e32 v116, 0
	v_mov_b32_e32 v123, 0
	v_mov_b32_e32 v122, 0
	v_mov_b32_e32 v121, 0
	v_mov_b32_e32 v120, 0
	s_and_saveexec_b64 s[26:27], s[64:65]
	s_cbranch_execz .LBB0_863
	v_ashrrev_i32_e32 v139, 31, v138
	v_lshlrev_b64 v[68:69], 6, v[138:139]
	v_lshl_add_u64 v[70:71], v[218:219], 0, v[68:69]
	v_lshl_add_u64 v[68:69], v[210:211], 0, v[68:69]
	global_load_dwordx4 v[120:123], v[68:69], off
	global_load_dwordx4 v[116:119], v[70:71], off

.LBB0_3260:
	s_add_u32 s12, s17, 0x27000000
	v_lshrrev_b32_e32 v7, 1, v2
	s_addc_u32 s13, s19, 0
	s_lshr_b32 s15, s15, 26
	v_and_b32_e32 v7, 24, v7
	v_and_b32_e32 v5, 15, v2
	s_add_i32 s15, s14, s15
	v_lshlrev_b32_e32 v9, 1, v7
	v_lshlrev_b32_e32 v2, 2, v2
	s_ashr_i32 s55, s15, 6
	v_lshl_or_b32 v143, s20, 6, v5
	v_lshl_or_b32 v5, v5, 6, v9
	s_lshl_b32 s15, s20, 13
	v_and_b32_e32 v2, 32, v2
	v_bitop3_b32 v9, v5, s15, v2 bitop3:0xde
	s_lshl_b32 s15, s21, 5
	s_and_b32 s19, s15, 0x60
	s_lshl_b32 s15, s19, 7
	s_cmp_gt_i32 s14, 63
	v_bitop3_b32 v147, v5, s15, v2 bitop3:0xde
	s_cselect_b64 s[14:15], -1, 0
	s_add_i32 s56, s55, -2
	s_cmpk_lt_u32 s16, 0x100
	v_or_b32_e32 v152, s19, v7
	v_readlane_b32 s19, v255, 3
	s_cselect_b64 s[16:17], -1, 0
	s_add_u32 s36, s19, s30
	v_readlane_b32 s19, v255, 4
	v_readlane_b32 s44, v254, 24
	s_addc_u32 s37, s19, s31
	s_mov_b32 s57, 0
	v_add_u32_e32 v153, 0, v9
	v_readlane_b32 s63, v254, 40
	v_readlane_b32 s64, v254, 42
	v_readlane_b32 s58, v254, 26
	v_readlane_b32 s59, v254, 45
	v_readlane_b32 s45, v254, 25
	s_mov_b64 s[42:43], s[26:27]
	s_mov_b32 s100, 0
	s_branch .LBB0_3263

.LBB0_3262:
	s_and_b64 vcc, exec, s[26:27]
	v_mov_b32_e32 v140, v156
	s_waitcnt vmcnt(8)
	v_mov_b32_e32 v144, v155
	v_mov_b32_e32 v142, v157
	v_mov_b32_e32 v146, v154
	s_mov_b32 s63, s58
	s_mov_b32 s64, s59
	s_mov_b32 s58, s61
	s_mov_b32 s59, s60
	s_mov_b64 s[26:27], s[42:43]
	s_cbranch_vccnz .LBB0_3282

.LBB0_3265:
	s_andn2_b64 vcc, exec, s[14:15]
	s_cbranch_vccnz .LBB0_3268
	v_mov_b32_e32 v141, v3
	v_mov_b32_e32 v145, v3
	s_add_u32 s19, s26, 0x100
	s_addc_u32 s20, s27, 0
	v_lshl_add_u64 v[148:149], s[36:37], 0, v[140:141]
	v_lshl_add_u64 v[150:151], s[36:37], 0, v[144:145]
	s_mov_b32 s21, 0
	s_mov_b64 s[26:27], 0
	s_cmp_eq_u32 s56, s21
	s_cselect_b64 vcc, -1, 0
	s_add_i32 s21, s21, 2
	s_add_u32 s30, s26, 0x100
	s_addc_u32 s31, s27, 0
	s_and_b64 s[22:23], vcc, exec
	s_cselect_b32 s23, 0, s30
	s_cselect_b32 s22, 0, s31
	s_add_u32 s40, s2, s23
	s_addc_u32 s41, s3, s22
	s_add_u32 s28, s19, s26
	s_addc_u32 s29, s20, s27
	s_add_i32 s65, 0, 0x10000
	s_and_b64 s[22:23], vcc, exec
	v_add_u32_e32 v141, s65, v147
	s_cselect_b32 s23, s43, s29
	s_cselect_b32 s22, s42, s28
	s_add_i32 s28, 0, 0x14000
	ds_read_b128 v[158:161], v141
	ds_read_b128 v[162:165], v141 offset:1024
	ds_read_b128 v[166:169], v141 offset:2048
	ds_read_b128 v[170:173], v141 offset:3072
	v_add_u32_e32 v141, s28, v147
	ds_read_b128 v[174:177], v141
	ds_read_b128 v[178:181], v141 offset:1024
	ds_read_b128 v[182:185], v141 offset:2048
	ds_read_b128 v[186:189], v141 offset:3072
	v_cndmask_b32_e32 v2, v142, v157, vcc
	v_cndmask_b32_e32 v141, v140, v156, vcc
	v_cndmask_b32_e32 v210, v146, v154, vcc
	v_cndmask_b32_e32 v145, v144, v155, vcc
	v_lshl_add_u64 v[212:213], v[148:149], 0, s[26:27]
	s_add_i32 m0, s49, 0xc000
	ds_read_b128 v[190:193], v153
	ds_read_b128 v[194:197], v153 offset:1024
	ds_read_b128 v[198:201], v153 offset:2048
	ds_read_b128 v[202:205], v153 offset:3072
	ds_read_b128 v[206:209], v153 offset:4096
	ds_read_b128 v[218:221], v153 offset:5120
	ds_read_b128 v[222:225], v153 offset:6144
	ds_read_b128 v[226:229], v153 offset:7168
	global_load_lds_dwordx4 v[212:213], off
	v_lshl_add_u64 v[212:213], v[150:151], 0, s[26:27]
	s_add_i32 m0, s49, 0xe000
	s_nop 0
	global_load_lds_dwordx4 v[212:213], off
	s_cmp_eq_u32 s100, 0
	s_cbranch_scc1 .Lmy_w10a
	s_waitcnt vmcnt(16)
	s_branch .Lmy_w10b

.Lmy_w10b:
	s_waitcnt lgkmcnt(0)
	s_barrier
	s_setprio 1
	v_mfma_f32_16x16x32_bf16 v[124:127], v[158:161], v[190:193], 0
	v_mfma_f32_16x16x32_bf16 v[120:123], v[166:169], v[190:193], 0
	v_mfma_f32_16x16x32_bf16 v[112:115], v[158:161], v[198:201], 0
	v_mfma_f32_16x16x32_bf16 v[104:107], v[166:169], v[198:201], 0
	v_mfma_f32_16x16x32_bf16 v[96:99], v[158:161], v[206:209], 0
	v_mfma_f32_16x16x32_bf16 v[88:91], v[166:169], v[206:209], 0
	v_mfma_f32_16x16x32_bf16 v[80:83], v[158:161], v[222:225], 0
	v_mfma_f32_16x16x32_bf16 v[72:75], v[166:169], v[222:225], 0
	v_mfma_f32_16x16x32_bf16 v[124:127], v[162:165], v[194:197], v[124:127]
	v_mfma_f32_16x16x32_bf16 v[120:123], v[170:173], v[194:197], v[120:123]
	v_mfma_f32_16x16x32_bf16 v[112:115], v[162:165], v[202:205], v[112:115]
	v_mfma_f32_16x16x32_bf16 v[104:107], v[170:173], v[202:205], v[104:107]
	v_mfma_f32_16x16x32_bf16 v[96:99], v[162:165], v[218:221], v[96:99]
	v_mfma_f32_16x16x32_bf16 v[88:91], v[170:173], v[218:221], v[88:91]
	v_mfma_f32_16x16x32_bf16 v[80:83], v[162:165], v[226:229], v[80:83]
	v_mfma_f32_16x16x32_bf16 v[72:75], v[170:173], v[226:229], v[72:75]
	s_setprio 0
	s_setprio 1
	v_mfma_f32_16x16x32_bf16 v[128:131], v[174:177], v[190:193], 0
	v_mfma_f32_16x16x32_bf16 v[116:119], v[182:185], v[190:193], 0
	v_mfma_f32_16x16x32_bf16 v[108:111], v[174:177], v[198:201], 0
	v_mfma_f32_16x16x32_bf16 v[100:103], v[182:185], v[198:201], 0
	v_mfma_f32_16x16x32_bf16 v[92:95], v[174:177], v[206:209], 0
	v_mfma_f32_16x16x32_bf16 v[84:87], v[182:185], v[206:209], 0
	v_mfma_f32_16x16x32_bf16 v[76:79], v[174:177], v[222:225], 0
	v_mfma_f32_16x16x32_bf16 v[68:71], v[182:185], v[222:225], 0
	v_mfma_f32_16x16x32_bf16 v[128:131], v[178:181], v[194:197], v[128:131]
	v_mfma_f32_16x16x32_bf16 v[116:119], v[186:189], v[194:197], v[116:119]
	v_mfma_f32_16x16x32_bf16 v[108:111], v[178:181], v[202:205], v[108:111]
	v_mfma_f32_16x16x32_bf16 v[100:103], v[186:189], v[202:205], v[100:103]
	v_mfma_f32_16x16x32_bf16 v[92:95], v[178:181], v[218:221], v[92:95]
	v_mfma_f32_16x16x32_bf16 v[84:87], v[186:189], v[218:221], v[84:87]
	v_mfma_f32_16x16x32_bf16 v[76:79], v[178:181], v[226:229], v[76:79]
	v_mfma_f32_16x16x32_bf16 v[68:71], v[186:189], v[226:229], v[68:71]
	s_barrier
	s_setprio 0
	s_add_i32 s26, s65, s47
	v_lshl_add_u64 v[212:213], s[22:23], 0, v[138:139]
	s_mov_b32 m0, s26
	ds_read_b128 v[190:193], v153 offset:16384
	ds_read_b128 v[194:197], v153 offset:17408
	ds_read_b128 v[198:201], v153 offset:18432
	ds_read_b128 v[202:205], v153 offset:19456
	ds_read_b128 v[206:209], v153 offset:20480
	ds_read_b128 v[218:221], v153 offset:21504
	ds_read_b128 v[222:225], v153 offset:22528
	ds_read_b128 v[226:229], v153 offset:23552
	global_load_lds_dwordx4 v[212:213], off
	s_add_i32 m0, s26, 0x2000
	v_lshl_add_u64 v[214:215], s[22:23], 0, v[136:137]
	s_add_u32 s22, s22, s6
	s_addc_u32 s23, s23, s7
	s_add_i32 s26, s28, s47
	global_load_lds_dwordx4 v[214:215], off
	v_lshl_add_u64 v[230:231], s[22:23], 0, v[138:139]
	s_mov_b32 m0, s26
	v_lshl_add_u64 v[240:241], s[22:23], 0, v[136:137]
	global_load_lds_dwordx4 v[230:231], off
	s_add_i32 m0, s26, 0x2000
	v_mov_b32_e32 v211, v3
	global_load_lds_dwordx4 v[240:241], off
	s_mov_b32 m0, s49
	v_lshl_add_u64 v[242:243], s[40:41], 0, v[2:3]
	global_load_lds_dwordx4 v2, s[40:41]
	s_mov_b32 m0, s50
	s_nop 0
	global_load_lds_dwordx4 v210, s[40:41]
	s_cmp_eq_u32 s100, 0
	s_cbranch_scc1 .Lmy_w11a
	s_waitcnt vmcnt(16)
	s_branch .Lmy_w11b

.Lmy_w11b:
	s_mov_b32 s100, 1
	s_waitcnt lgkmcnt(0)
	v_lshl_add_u64 v[210:211], s[40:41], 0, v[210:211]
	s_barrier
	s_setprio 1
	s_waitcnt lgkmcnt(0)
	v_mfma_f32_16x16x32_bf16 v[64:67], v[158:161], v[190:193], 0
	v_mfma_f32_16x16x32_bf16 v[56:59], v[166:169], v[190:193], 0
	v_mfma_f32_16x16x32_bf16 v[48:51], v[158:161], v[198:201], 0
	v_mfma_f32_16x16x32_bf16 v[40:43], v[166:169], v[198:201], 0
	v_mfma_f32_16x16x32_bf16 v[32:35], v[158:161], v[206:209], 0
	v_mfma_f32_16x16x32_bf16 v[24:27], v[166:169], v[206:209], 0
	v_mfma_f32_16x16x32_bf16 v[16:19], v[158:161], v[222:225], 0
	v_mfma_f32_16x16x32_bf16 v[8:11], v[166:169], v[222:225], 0
	v_mfma_f32_16x16x32_bf16 v[64:67], v[162:165], v[194:197], v[64:67]
	v_mfma_f32_16x16x32_bf16 v[56:59], v[170:173], v[194:197], v[56:59]
	v_mfma_f32_16x16x32_bf16 v[48:51], v[162:165], v[202:205], v[48:51]
	v_mfma_f32_16x16x32_bf16 v[40:43], v[170:173], v[202:205], v[40:43]
	v_mfma_f32_16x16x32_bf16 v[32:35], v[162:165], v[218:221], v[32:35]
	v_mfma_f32_16x16x32_bf16 v[24:27], v[170:173], v[218:221], v[24:27]
	v_mfma_f32_16x16x32_bf16 v[16:19], v[162:165], v[226:229], v[16:19]
	v_mfma_f32_16x16x32_bf16 v[8:11], v[170:173], v[226:229], v[8:11]
	s_setprio 0
	s_setprio 1
	v_mfma_f32_16x16x32_bf16 v[60:63], v[174:177], v[190:193], 0
	v_mfma_f32_16x16x32_bf16 v[52:55], v[182:185], v[190:193], 0
	v_mfma_f32_16x16x32_bf16 v[44:47], v[174:177], v[198:201], 0
	v_mfma_f32_16x16x32_bf16 v[36:39], v[182:185], v[198:201], 0
	v_mfma_f32_16x16x32_bf16 v[28:31], v[174:177], v[206:209], 0
	v_mfma_f32_16x16x32_bf16 v[20:23], v[182:185], v[206:209], 0
	v_mfma_f32_16x16x32_bf16 v[12:15], v[174:177], v[222:225], 0
	v_mfma_f32_16x16x32_bf16 v[4:7], v[182:185], v[222:225], 0
	v_mfma_f32_16x16x32_bf16 v[60:63], v[178:181], v[194:197], v[60:63]
	v_mfma_f32_16x16x32_bf16 v[52:55], v[186:189], v[194:197], v[52:55]
	v_mfma_f32_16x16x32_bf16 v[44:47], v[178:181], v[202:205], v[44:47]
	v_mfma_f32_16x16x32_bf16 v[36:39], v[186:189], v[202:205], v[36:39]
	v_mfma_f32_16x16x32_bf16 v[28:31], v[178:181], v[218:221], v[28:31]
	v_mfma_f32_16x16x32_bf16 v[20:23], v[186:189], v[218:221], v[20:23]
	v_mfma_f32_16x16x32_bf16 v[12:15], v[178:181], v[226:229], v[12:15]
	v_mfma_f32_16x16x32_bf16 v[4:7], v[186:189], v[226:229], v[4:7]
	s_barrier
	s_setprio 0
	s_add_i32 s22, 0, 0x18000
	v_add_u32_e32 v2, s22, v147
	s_add_i32 s23, 0, 0x1c000
	ds_read_b128 v[158:161], v2
	ds_read_b128 v[162:165], v2 offset:1024
	ds_read_b128 v[166:169], v2 offset:2048
	ds_read_b128 v[170:173], v2 offset:3072
	v_add_u32_e32 v2, s23, v147
	ds_read_b128 v[174:177], v2
	ds_read_b128 v[178:181], v2 offset:1024
	ds_read_b128 v[182:185], v2 offset:2048
	ds_read_b128 v[186:189], v2 offset:3072
	s_mov_b32 m0, s51
	ds_read_b128 v[190:193], v153 offset:32768
	ds_read_b128 v[194:197], v153 offset:33792
	ds_read_b128 v[198:201], v153 offset:34816
	ds_read_b128 v[202:205], v153 offset:35840
	ds_read_b128 v[206:209], v153 offset:36864
	ds_read_b128 v[218:221], v153 offset:37888
	ds_read_b128 v[222:225], v153 offset:38912
	ds_read_b128 v[226:229], v153 offset:39936
	global_load_lds_dwordx4 v141, s[40:41]
	s_mov_b32 m0, s52
	s_nop 0
	global_load_lds_dwordx4 v145, s[40:41]
	s_waitcnt vmcnt(8)
	s_waitcnt lgkmcnt(0)
	s_barrier
	s_setprio 1
	v_mfma_f32_16x16x32_bf16 v[124:127], v[158:161], v[190:193], v[124:127]
	v_mfma_f32_16x16x32_bf16 v[120:123], v[166:169], v[190:193], v[120:123]
	v_mfma_f32_16x16x32_bf16 v[112:115], v[158:161], v[198:201], v[112:115]
	v_mfma_f32_16x16x32_bf16 v[104:107], v[166:169], v[198:201], v[104:107]
	v_mfma_f32_16x16x32_bf16 v[96:99], v[158:161], v[206:209], v[96:99]
	v_mfma_f32_16x16x32_bf16 v[88:91], v[166:169], v[206:209], v[88:91]
	v_mfma_f32_16x16x32_bf16 v[80:83], v[158:161], v[222:225], v[80:83]
	v_mfma_f32_16x16x32_bf16 v[72:75], v[166:169], v[222:225], v[72:75]
	v_mfma_f32_16x16x32_bf16 v[124:127], v[162:165], v[194:197], v[124:127]
	v_mfma_f32_16x16x32_bf16 v[120:123], v[170:173], v[194:197], v[120:123]
	v_mfma_f32_16x16x32_bf16 v[112:115], v[162:165], v[202:205], v[112:115]
	v_mfma_f32_16x16x32_bf16 v[104:107], v[170:173], v[202:205], v[104:107]
	v_mfma_f32_16x16x32_bf16 v[96:99], v[162:165], v[218:221], v[96:99]
	v_mfma_f32_16x16x32_bf16 v[88:91], v[170:173], v[218:221], v[88:91]
	v_mfma_f32_16x16x32_bf16 v[80:83], v[162:165], v[226:229], v[80:83]
	v_mfma_f32_16x16x32_bf16 v[72:75], v[170:173], v[226:229], v[72:75]
	s_setprio 0
	s_setprio 1
	v_mfma_f32_16x16x32_bf16 v[128:131], v[174:177], v[190:193], v[128:131]
	v_mfma_f32_16x16x32_bf16 v[116:119], v[182:185], v[190:193], v[116:119]
	v_mfma_f32_16x16x32_bf16 v[108:111], v[174:177], v[198:201], v[108:111]
	v_mfma_f32_16x16x32_bf16 v[100:103], v[182:185], v[198:201], v[100:103]
	v_mfma_f32_16x16x32_bf16 v[92:95], v[174:177], v[206:209], v[92:95]
	v_mfma_f32_16x16x32_bf16 v[84:87], v[182:185], v[206:209], v[84:87]
	v_mfma_f32_16x16x32_bf16 v[76:79], v[174:177], v[222:225], v[76:79]
	v_mfma_f32_16x16x32_bf16 v[68:71], v[182:185], v[222:225], v[68:71]
	v_mfma_f32_16x16x32_bf16 v[128:131], v[178:181], v[194:197], v[128:131]
	v_mfma_f32_16x16x32_bf16 v[116:119], v[186:189], v[194:197], v[116:119]
	v_mfma_f32_16x16x32_bf16 v[108:111], v[178:181], v[202:205], v[108:111]
	v_mfma_f32_16x16x32_bf16 v[100:103], v[186:189], v[202:205], v[100:103]
	v_mfma_f32_16x16x32_bf16 v[92:95], v[178:181], v[218:221], v[92:95]
	v_mfma_f32_16x16x32_bf16 v[84:87], v[186:189], v[218:221], v[84:87]
	v_mfma_f32_16x16x32_bf16 v[76:79], v[178:181], v[226:229], v[76:79]
	v_mfma_f32_16x16x32_bf16 v[68:71], v[186:189], v[226:229], v[68:71]
	s_barrier
	s_setprio 0
	s_add_i32 s22, s22, s47
	v_lshl_add_u64 v[212:213], v[212:213], 0, s[24:25]
	s_mov_b32 m0, s22
	ds_read_b128 v[190:193], v153 offset:49152
	ds_read_b128 v[194:197], v153 offset:50176
	ds_read_b128 v[198:201], v153 offset:51200
	ds_read_b128 v[202:205], v153 offset:52224
	ds_read_b128 v[206:209], v153 offset:53248
	ds_read_b128 v[218:221], v153 offset:54272
	ds_read_b128 v[222:225], v153 offset:55296
	ds_read_b128 v[226:229], v153 offset:56320
	global_load_lds_dwordx4 v[212:213], off
	v_lshl_add_u64 v[212:213], v[214:215], 0, s[24:25]
	s_add_i32 m0, s22, 0x2000
	s_add_i32 s22, s23, s47
	global_load_lds_dwordx4 v[212:213], off
	v_lshl_add_u64 v[212:213], v[230:231], 0, s[24:25]
	s_mov_b32 m0, s22
	v_lshl_add_u64 v[210:211], v[210:211], 0, s[24:25]
	global_load_lds_dwordx4 v[212:213], off
	v_lshl_add_u64 v[212:213], v[240:241], 0, s[24:25]
	s_add_i32 m0, s22, 0x2000
	s_nop 0
	global_load_lds_dwordx4 v[212:213], off
	v_lshl_add_u64 v[212:213], v[242:243], 0, s[24:25]
	s_mov_b32 m0, s53
	s_nop 0
	global_load_lds_dwordx4 v[212:213], off
	s_mov_b32 m0, s54
	s_nop 0
	global_load_lds_dwordx4 v[210:211], off
	s_waitcnt vmcnt(8)
	s_waitcnt lgkmcnt(0)
	s_barrier
	s_setprio 1
	v_mfma_f32_16x16x32_bf16 v[64:67], v[158:161], v[190:193], v[64:67]
	v_mfma_f32_16x16x32_bf16 v[56:59], v[166:169], v[190:193], v[56:59]
	v_mfma_f32_16x16x32_bf16 v[48:51], v[158:161], v[198:201], v[48:51]
	v_mfma_f32_16x16x32_bf16 v[40:43], v[166:169], v[198:201], v[40:43]
	v_mfma_f32_16x16x32_bf16 v[32:35], v[158:161], v[206:209], v[32:35]
	v_mfma_f32_16x16x32_bf16 v[24:27], v[166:169], v[206:209], v[24:27]
	v_mfma_f32_16x16x32_bf16 v[16:19], v[158:161], v[222:225], v[16:19]
	v_mfma_f32_16x16x32_bf16 v[8:11], v[166:169], v[222:225], v[8:11]
	v_mfma_f32_16x16x32_bf16 v[64:67], v[162:165], v[194:197], v[64:67]
	v_mfma_f32_16x16x32_bf16 v[56:59], v[170:173], v[194:197], v[56:59]
	v_mfma_f32_16x16x32_bf16 v[48:51], v[162:165], v[202:205], v[48:51]
	v_mfma_f32_16x16x32_bf16 v[40:43], v[170:173], v[202:205], v[40:43]
	v_mfma_f32_16x16x32_bf16 v[32:35], v[162:165], v[218:221], v[32:35]
	v_mfma_f32_16x16x32_bf16 v[24:27], v[170:173], v[218:221], v[24:27]
	v_mfma_f32_16x16x32_bf16 v[16:19], v[162:165], v[226:229], v[16:19]
	v_mfma_f32_16x16x32_bf16 v[8:11], v[170:173], v[226:229], v[8:11]
	s_setprio 0
	s_setprio 1
	v_mfma_f32_16x16x32_bf16 v[60:63], v[174:177], v[190:193], v[60:63]
	v_mfma_f32_16x16x32_bf16 v[52:55], v[182:185], v[190:193], v[52:55]
	v_mfma_f32_16x16x32_bf16 v[44:47], v[174:177], v[198:201], v[44:47]
	v_mfma_f32_16x16x32_bf16 v[36:39], v[182:185], v[198:201], v[36:39]
	v_mfma_f32_16x16x32_bf16 v[28:31], v[174:177], v[206:209], v[28:31]
	v_mfma_f32_16x16x32_bf16 v[20:23], v[182:185], v[206:209], v[20:23]
	v_mfma_f32_16x16x32_bf16 v[12:15], v[174:177], v[222:225], v[12:15]
	v_mfma_f32_16x16x32_bf16 v[4:7], v[182:185], v[222:225], v[4:7]
	v_mfma_f32_16x16x32_bf16 v[60:63], v[178:181], v[194:197], v[60:63]
	v_mfma_f32_16x16x32_bf16 v[52:55], v[186:189], v[194:197], v[52:55]
	v_mfma_f32_16x16x32_bf16 v[44:47], v[178:181], v[202:205], v[44:47]
	v_mfma_f32_16x16x32_bf16 v[36:39], v[186:189], v[202:205], v[36:39]
	v_mfma_f32_16x16x32_bf16 v[28:31], v[178:181], v[218:221], v[28:31]
	v_mfma_f32_16x16x32_bf16 v[20:23], v[186:189], v[218:221], v[20:23]
	v_mfma_f32_16x16x32_bf16 v[12:15], v[178:181], v[226:229], v[12:15]
	v_mfma_f32_16x16x32_bf16 v[4:7], v[186:189], v[226:229], v[4:7]
	s_barrier
	s_setprio 0
	s_cmp_ge_i32 s21, s55
	s_mov_b64 s[26:27], s[30:31]
	s_cbranch_scc1 .LBB0_3268

.LBB0_3276:
	s_mov_b32 s98, 0xbfb8aa3b
	s_mov_b32 s99, 0xbfb8aa3b
	v_mov_b32_e32 v166, 1.0
	v_mov_b32_e32 v167, 1.0
	v_lshl_add_u32 v140, s64, 8, v143
	s_lshl_b32 s19, s63, 7
	s_and_b32 s19, s19, 0x380
	v_ashrrev_i32_e32 v141, 31, v140
	v_lshlrev_b64 v[168:169], 11, v[140:141]
	v_lshl_add_u64 v[168:169], s[12:13], 0, v[168:169]
	v_or_b32_e32 v2, s19, v152
	v_lshlrev_b32_e32 v2, 1, v2
	v_lshl_add_u64 v[168:169], v[168:169], 0, v[2:3]
	v_pk_mul_f32 v[158:159], v[124:125], s[98:99]
	v_pk_mul_f32 v[160:161], v[126:127], s[98:99]
	v_pk_mul_f32 v[162:163], v[120:121], s[98:99]
	v_pk_mul_f32 v[164:165], v[122:123], s[98:99]
	v_exp_f32_e32 v158, v158
	v_exp_f32_e32 v159, v159
	v_exp_f32_e32 v160, v160
	v_exp_f32_e32 v161, v161
	v_exp_f32_e32 v162, v162
	v_exp_f32_e32 v163, v163
	v_exp_f32_e32 v164, v164
	v_exp_f32_e32 v165, v165
	v_pk_add_f32 v[158:159], v[158:159], v[166:167]
	v_pk_add_f32 v[160:161], v[160:161], v[166:167]
	v_pk_add_f32 v[162:163], v[162:163], v[166:167]
	v_pk_add_f32 v[164:165], v[164:165], v[166:167]
	v_rcp_f32_e32 v158, v158
	v_rcp_f32_e32 v159, v159
	v_rcp_f32_e32 v160, v160
	v_rcp_f32_e32 v161, v161
	v_rcp_f32_e32 v162, v162
	v_rcp_f32_e32 v163, v163
	v_rcp_f32_e32 v164, v164
	v_rcp_f32_e32 v165, v165
	v_pk_mul_f32 v[158:159], v[124:125], v[158:159]
	v_pk_mul_f32 v[160:161], v[126:127], v[160:161]
	v_pk_mul_f32 v[162:163], v[120:121], v[162:163]
	v_pk_mul_f32 v[164:165], v[122:123], v[164:165]
	v_pk_mul_f32 v[158:159], v[128:129], v[158:159]
	v_pk_mul_f32 v[160:161], v[130:131], v[160:161]
	v_pk_mul_f32 v[162:163], v[116:117], v[162:163]
	v_pk_mul_f32 v[164:165], v[118:119], v[164:165]
	v_cvt_pk_bf16_f32 v124, v158, v159
	v_cvt_pk_bf16_f32 v125, v160, v161
	v_cvt_pk_bf16_f32 v126, v162, v163
	v_cvt_pk_bf16_f32 v127, v164, v165
	global_store_dwordx4 v[168:169], v[124:127], off
	v_pk_mul_f32 v[158:159], v[112:113], s[98:99]
	v_pk_mul_f32 v[160:161], v[114:115], s[98:99]
	v_pk_mul_f32 v[162:163], v[104:105], s[98:99]
	v_pk_mul_f32 v[164:165], v[106:107], s[98:99]
	v_exp_f32_e32 v158, v158
	v_exp_f32_e32 v159, v159
	v_exp_f32_e32 v160, v160
	v_exp_f32_e32 v161, v161
	v_exp_f32_e32 v162, v162
	v_exp_f32_e32 v163, v163
	v_exp_f32_e32 v164, v164
	v_exp_f32_e32 v165, v165
	v_pk_add_f32 v[158:159], v[158:159], v[166:167]
	v_pk_add_f32 v[160:161], v[160:161], v[166:167]
	v_pk_add_f32 v[162:163], v[162:163], v[166:167]
	v_pk_add_f32 v[164:165], v[164:165], v[166:167]
	v_rcp_f32_e32 v158, v158
	v_rcp_f32_e32 v159, v159
	v_rcp_f32_e32 v160, v160
	v_rcp_f32_e32 v161, v161
	v_rcp_f32_e32 v162, v162
	v_rcp_f32_e32 v163, v163
	v_rcp_f32_e32 v164, v164
	v_rcp_f32_e32 v165, v165
	v_pk_mul_f32 v[158:159], v[112:113], v[158:159]
	v_pk_mul_f32 v[160:161], v[114:115], v[160:161]
	v_pk_mul_f32 v[162:163], v[104:105], v[162:163]
	v_pk_mul_f32 v[164:165], v[106:107], v[164:165]
	v_pk_mul_f32 v[158:159], v[108:109], v[158:159]
	v_pk_mul_f32 v[160:161], v[110:111], v[160:161]
	v_pk_mul_f32 v[162:163], v[100:101], v[162:163]
	v_pk_mul_f32 v[164:165], v[102:103], v[164:165]
	v_cvt_pk_bf16_f32 v112, v158, v159
	v_cvt_pk_bf16_f32 v113, v160, v161
	v_cvt_pk_bf16_f32 v114, v162, v163
	v_cvt_pk_bf16_f32 v115, v164, v165
	v_add_co_u32_e32 v108, vcc, 0x8000, v168
	s_nop 1
	v_addc_co_u32_e32 v109, vcc, 0, v169, vcc
	global_store_dwordx4 v[108:109], v[112:115], off
	v_pk_mul_f32 v[158:159], v[96:97], s[98:99]
	v_pk_mul_f32 v[160:161], v[98:99], s[98:99]
	v_pk_mul_f32 v[162:163], v[88:89], s[98:99]
	v_pk_mul_f32 v[164:165], v[90:91], s[98:99]
	v_exp_f32_e32 v158, v158
	v_exp_f32_e32 v159, v159
	v_exp_f32_e32 v160, v160
	v_exp_f32_e32 v161, v161
	v_exp_f32_e32 v162, v162
	v_exp_f32_e32 v163, v163
	v_exp_f32_e32 v164, v164
	v_exp_f32_e32 v165, v165
	v_pk_add_f32 v[158:159], v[158:159], v[166:167]
	v_pk_add_f32 v[160:161], v[160:161], v[166:167]
	v_pk_add_f32 v[162:163], v[162:163], v[166:167]
	v_pk_add_f32 v[164:165], v[164:165], v[166:167]
	v_rcp_f32_e32 v158, v158
	v_rcp_f32_e32 v159, v159
	v_rcp_f32_e32 v160, v160
	v_rcp_f32_e32 v161, v161
	v_rcp_f32_e32 v162, v162
	v_rcp_f32_e32 v163, v163
	v_rcp_f32_e32 v164, v164
	v_rcp_f32_e32 v165, v165
	v_pk_mul_f32 v[158:159], v[96:97], v[158:159]
	v_pk_mul_f32 v[160:161], v[98:99], v[160:161]
	v_pk_mul_f32 v[162:163], v[88:89], v[162:163]
	v_pk_mul_f32 v[164:165], v[90:91], v[164:165]
	v_pk_mul_f32 v[158:159], v[92:93], v[158:159]
	v_pk_mul_f32 v[160:161], v[94:95], v[160:161]
	v_pk_mul_f32 v[162:163], v[84:85], v[162:163]
	v_pk_mul_f32 v[164:165], v[86:87], v[164:165]
	v_cvt_pk_bf16_f32 v96, v158, v159
	v_cvt_pk_bf16_f32 v97, v160, v161
	v_cvt_pk_bf16_f32 v98, v162, v163
	v_cvt_pk_bf16_f32 v99, v164, v165
	v_add_co_u32_e32 v92, vcc, 0x10000, v168
	s_nop 1
	v_addc_co_u32_e32 v93, vcc, 0, v169, vcc
	global_store_dwordx4 v[92:93], v[96:99], off
	v_pk_mul_f32 v[158:159], v[80:81], s[98:99]
	v_pk_mul_f32 v[160:161], v[82:83], s[98:99]
	v_pk_mul_f32 v[162:163], v[72:73], s[98:99]
	v_pk_mul_f32 v[164:165], v[74:75], s[98:99]
	v_exp_f32_e32 v158, v158
	v_exp_f32_e32 v159, v159
	v_exp_f32_e32 v160, v160
	v_exp_f32_e32 v161, v161
	v_exp_f32_e32 v162, v162
	v_exp_f32_e32 v163, v163
	v_exp_f32_e32 v164, v164
	v_exp_f32_e32 v165, v165
	v_pk_add_f32 v[158:159], v[158:159], v[166:167]
	v_pk_add_f32 v[160:161], v[160:161], v[166:167]
	v_pk_add_f32 v[162:163], v[162:163], v[166:167]
	v_pk_add_f32 v[164:165], v[164:165], v[166:167]
	v_rcp_f32_e32 v158, v158
	v_rcp_f32_e32 v159, v159
	v_rcp_f32_e32 v160, v160
	v_rcp_f32_e32 v161, v161
	v_rcp_f32_e32 v162, v162
	v_rcp_f32_e32 v163, v163
	v_rcp_f32_e32 v164, v164
	v_rcp_f32_e32 v165, v165
	v_pk_mul_f32 v[158:159], v[80:81], v[158:159]
	v_pk_mul_f32 v[160:161], v[82:83], v[160:161]
	v_pk_mul_f32 v[162:163], v[72:73], v[162:163]
	v_pk_mul_f32 v[164:165], v[74:75], v[164:165]
	v_pk_mul_f32 v[158:159], v[76:77], v[158:159]
	v_pk_mul_f32 v[160:161], v[78:79], v[160:161]
	v_pk_mul_f32 v[162:163], v[68:69], v[162:163]
	v_pk_mul_f32 v[164:165], v[70:71], v[164:165]
	v_cvt_pk_bf16_f32 v80, v158, v159
	v_cvt_pk_bf16_f32 v81, v160, v161
	v_cvt_pk_bf16_f32 v82, v162, v163
	v_cvt_pk_bf16_f32 v83, v164, v165
	v_add_co_u32_e32 v76, vcc, 0x18000, v168
	s_nop 1
	v_addc_co_u32_e32 v77, vcc, 0, v169, vcc
	global_store_dwordx4 v[76:77], v[80:83], off
	v_pk_mul_f32 v[158:159], v[64:65], s[98:99]
	v_pk_mul_f32 v[160:161], v[66:67], s[98:99]
	v_pk_mul_f32 v[162:163], v[56:57], s[98:99]
	v_pk_mul_f32 v[164:165], v[58:59], s[98:99]
	v_exp_f32_e32 v158, v158
	v_exp_f32_e32 v159, v159
	v_exp_f32_e32 v160, v160
	v_exp_f32_e32 v161, v161
	v_exp_f32_e32 v162, v162
	v_exp_f32_e32 v163, v163
	v_exp_f32_e32 v164, v164
	v_exp_f32_e32 v165, v165
	v_pk_add_f32 v[158:159], v[158:159], v[166:167]
	v_pk_add_f32 v[160:161], v[160:161], v[166:167]
	v_pk_add_f32 v[162:163], v[162:163], v[166:167]
	v_pk_add_f32 v[164:165], v[164:165], v[166:167]
	v_rcp_f32_e32 v158, v158
	v_rcp_f32_e32 v159, v159
	v_rcp_f32_e32 v160, v160
	v_rcp_f32_e32 v161, v161
	v_rcp_f32_e32 v162, v162
	v_rcp_f32_e32 v163, v163
	v_rcp_f32_e32 v164, v164
	v_rcp_f32_e32 v165, v165
	v_pk_mul_f32 v[158:159], v[64:65], v[158:159]
	v_pk_mul_f32 v[160:161], v[66:67], v[160:161]
	v_pk_mul_f32 v[162:163], v[56:57], v[162:163]
	v_pk_mul_f32 v[164:165], v[58:59], v[164:165]
	v_pk_mul_f32 v[158:159], v[60:61], v[158:159]
	v_pk_mul_f32 v[160:161], v[62:63], v[160:161]
	v_pk_mul_f32 v[162:163], v[52:53], v[162:163]
	v_pk_mul_f32 v[164:165], v[54:55], v[164:165]
	v_cvt_pk_bf16_f32 v64, v158, v159
	v_cvt_pk_bf16_f32 v65, v160, v161
	v_cvt_pk_bf16_f32 v66, v162, v163
	v_cvt_pk_bf16_f32 v67, v164, v165
	v_add_co_u32_e32 v60, vcc, 0x40000, v168
	s_nop 1
	v_addc_co_u32_e32 v61, vcc, 0, v169, vcc
	global_store_dwordx4 v[60:61], v[64:67], off
	v_pk_mul_f32 v[158:159], v[48:49], s[98:99]
	v_pk_mul_f32 v[160:161], v[50:51], s[98:99]
	v_pk_mul_f32 v[162:163], v[40:41], s[98:99]
	v_pk_mul_f32 v[164:165], v[42:43], s[98:99]
	v_exp_f32_e32 v158, v158
	v_exp_f32_e32 v159, v159
	v_exp_f32_e32 v160, v160
	v_exp_f32_e32 v161, v161
	v_exp_f32_e32 v162, v162
	v_exp_f32_e32 v163, v163
	v_exp_f32_e32 v164, v164
	v_exp_f32_e32 v165, v165
	v_pk_add_f32 v[158:159], v[158:159], v[166:167]
	v_pk_add_f32 v[160:161], v[160:161], v[166:167]
	v_pk_add_f32 v[162:163], v[162:163], v[166:167]
	v_pk_add_f32 v[164:165], v[164:165], v[166:167]
	v_rcp_f32_e32 v158, v158
	v_rcp_f32_e32 v159, v159
	v_rcp_f32_e32 v160, v160
	v_rcp_f32_e32 v161, v161
	v_rcp_f32_e32 v162, v162
	v_rcp_f32_e32 v163, v163
	v_rcp_f32_e32 v164, v164
	v_rcp_f32_e32 v165, v165
	v_pk_mul_f32 v[158:159], v[48:49], v[158:159]
	v_pk_mul_f32 v[160:161], v[50:51], v[160:161]
	v_pk_mul_f32 v[162:163], v[40:41], v[162:163]
	v_pk_mul_f32 v[164:165], v[42:43], v[164:165]
	v_pk_mul_f32 v[158:159], v[44:45], v[158:159]
	v_pk_mul_f32 v[160:161], v[46:47], v[160:161]
	v_pk_mul_f32 v[162:163], v[36:37], v[162:163]
	v_pk_mul_f32 v[164:165], v[38:39], v[164:165]
	v_cvt_pk_bf16_f32 v48, v158, v159
	v_cvt_pk_bf16_f32 v49, v160, v161
	v_cvt_pk_bf16_f32 v50, v162, v163
	v_cvt_pk_bf16_f32 v51, v164, v165
	v_add_co_u32_e32 v44, vcc, 0x48000, v168
	s_nop 1
	v_addc_co_u32_e32 v45, vcc, 0, v169, vcc
	global_store_dwordx4 v[44:45], v[48:51], off
	v_pk_mul_f32 v[158:159], v[32:33], s[98:99]
	v_pk_mul_f32 v[160:161], v[34:35], s[98:99]
	v_pk_mul_f32 v[162:163], v[24:25], s[98:99]
	v_pk_mul_f32 v[164:165], v[26:27], s[98:99]
	v_exp_f32_e32 v158, v158
	v_exp_f32_e32 v159, v159
	v_exp_f32_e32 v160, v160
	v_exp_f32_e32 v161, v161
	v_exp_f32_e32 v162, v162
	v_exp_f32_e32 v163, v163
	v_exp_f32_e32 v164, v164
	v_exp_f32_e32 v165, v165
	v_pk_add_f32 v[158:159], v[158:159], v[166:167]
	v_pk_add_f32 v[160:161], v[160:161], v[166:167]
	v_pk_add_f32 v[162:163], v[162:163], v[166:167]
	v_pk_add_f32 v[164:165], v[164:165], v[166:167]
	v_rcp_f32_e32 v158, v158
	v_rcp_f32_e32 v159, v159
	v_rcp_f32_e32 v160, v160
	v_rcp_f32_e32 v161, v161
	v_rcp_f32_e32 v162, v162
	v_rcp_f32_e32 v163, v163
	v_rcp_f32_e32 v164, v164
	v_rcp_f32_e32 v165, v165
	v_pk_mul_f32 v[158:159], v[32:33], v[158:159]
	v_pk_mul_f32 v[160:161], v[34:35], v[160:161]
	v_pk_mul_f32 v[162:163], v[24:25], v[162:163]
	v_pk_mul_f32 v[164:165], v[26:27], v[164:165]
	v_pk_mul_f32 v[158:159], v[28:29], v[158:159]
	v_pk_mul_f32 v[160:161], v[30:31], v[160:161]
	v_pk_mul_f32 v[162:163], v[20:21], v[162:163]
	v_pk_mul_f32 v[164:165], v[22:23], v[164:165]
	v_cvt_pk_bf16_f32 v32, v158, v159
	v_cvt_pk_bf16_f32 v33, v160, v161
	v_cvt_pk_bf16_f32 v34, v162, v163
	v_cvt_pk_bf16_f32 v35, v164, v165
	v_add_co_u32_e32 v28, vcc, 0x50000, v168
	s_nop 1
	v_addc_co_u32_e32 v29, vcc, 0, v169, vcc
	global_store_dwordx4 v[28:29], v[32:35], off
	v_pk_mul_f32 v[158:159], v[16:17], s[98:99]
	v_pk_mul_f32 v[160:161], v[18:19], s[98:99]
	v_pk_mul_f32 v[162:163], v[8:9], s[98:99]
	v_pk_mul_f32 v[164:165], v[10:11], s[98:99]
	v_exp_f32_e32 v158, v158
	v_exp_f32_e32 v159, v159
	v_exp_f32_e32 v160, v160
	v_exp_f32_e32 v161, v161
	v_exp_f32_e32 v162, v162
	v_exp_f32_e32 v163, v163
	v_exp_f32_e32 v164, v164
	v_exp_f32_e32 v165, v165
	v_pk_add_f32 v[158:159], v[158:159], v[166:167]
	v_pk_add_f32 v[160:161], v[160:161], v[166:167]
	v_pk_add_f32 v[162:163], v[162:163], v[166:167]
	v_pk_add_f32 v[164:165], v[164:165], v[166:167]
	v_rcp_f32_e32 v158, v158
	v_rcp_f32_e32 v159, v159
	v_rcp_f32_e32 v160, v160
	v_rcp_f32_e32 v161, v161
	v_rcp_f32_e32 v162, v162
	v_rcp_f32_e32 v163, v163
	v_rcp_f32_e32 v164, v164
	v_rcp_f32_e32 v165, v165
	v_pk_mul_f32 v[158:159], v[16:17], v[158:159]
	v_pk_mul_f32 v[160:161], v[18:19], v[160:161]
	v_pk_mul_f32 v[162:163], v[8:9], v[162:163]
	v_pk_mul_f32 v[164:165], v[10:11], v[164:165]
	v_pk_mul_f32 v[158:159], v[12:13], v[158:159]
	v_pk_mul_f32 v[160:161], v[14:15], v[160:161]
	v_pk_mul_f32 v[162:163], v[4:5], v[162:163]
	v_pk_mul_f32 v[164:165], v[6:7], v[164:165]
	v_cvt_pk_bf16_f32 v16, v158, v159
	v_cvt_pk_bf16_f32 v17, v160, v161
	v_cvt_pk_bf16_f32 v18, v162, v163
	v_cvt_pk_bf16_f32 v19, v164, v165
	v_add_co_u32_e32 v12, vcc, 0x58000, v168
	s_nop 1
	v_addc_co_u32_e32 v13, vcc, 0, v169, vcc
	global_store_dwordx4 v[12:13], v[16:19], off
	s_and_b64 vcc, exec, s[38:39]
	s_cbranch_vccnz .LBB0_3281
	s_and_b64 vcc, exec, s[40:41]
	v_mov_b32_e32 v4, v157
	v_mov_b32_e32 v8, v154
	v_mov_b32_e32 v6, v156
	v_mov_b32_e32 v10, v155
	s_cbranch_vccnz .LBB0_3279
	s_waitcnt vmcnt(8)
	v_mad_u64_u32 v[4:5], s[20:21], v142, s48, v[132:133]
	v_mad_u64_u32 v[6:7], s[20:21], v145, s48, v[132:133]
	v_mad_u64_u32 v[8:9], s[20:21], v144, s48, v[134:135]
	v_mad_u64_u32 v[10:11], s[20:21], v146, s48, v[134:135]

.LBB0_3488:
	s_add_u32 s8, s8, 0x2b000000
	s_addc_u32 s9, s9, 0
	s_add_i32 m0, s42, 0x18000
	v_lshl_add_u64 v[4:5], v[4:5], 0, s[24:25]
	s_waitcnt vmcnt(2)
	s_barrier
	global_load_lds_dwordx4 v[4:5], off
	v_lshl_add_u64 v[4:5], v[6:7], 0, s[24:25]
	s_add_i32 m0, s42, 0x1a000
	s_add_i32 s47, s42, 0x8000
	global_load_lds_dwordx4 v[4:5], off
	v_lshl_add_u64 v[4:5], v[12:13], 0, s[24:25]
	s_mov_b32 m0, s47
	s_add_i32 s48, s42, 0xa000
	global_load_lds_dwordx4 v[4:5], off
	v_lshl_add_u64 v[4:5], v[14:15], 0, s[24:25]
	s_mov_b32 m0, s48
	v_lshrrev_b32_e32 v23, 1, v21
	global_load_lds_dwordx4 v[4:5], off
	s_add_i32 m0, s42, 0x1c000
	v_lshl_add_u64 v[4:5], v[8:9], 0, s[24:25]
	global_load_lds_dwordx4 v[4:5], off
	v_lshl_add_u64 v[4:5], v[10:11], 0, s[24:25]
	s_add_i32 m0, s42, 0x1e000
	s_lshr_b32 s11, s11, 26
	global_load_lds_dwordx4 v[4:5], off
	v_and_b32_e32 v23, 24, v23
	v_and_b32_e32 v22, 15, v21
	s_add_i32 s11, s10, s11
	v_lshlrev_b32_e32 v24, 1, v23
	v_lshlrev_b32_e32 v21, 2, v21
	s_ashr_i32 s46, s11, 6
	v_lshl_or_b32 v144, s14, 6, v22
	v_lshl_or_b32 v22, v22, 6, v24
	s_lshl_b32 s11, s14, 13
	v_and_b32_e32 v21, 32, v21
	v_bitop3_b32 v24, v22, s11, v21 bitop3:0xde
	s_lshl_b32 s11, s13, 5
	s_and_b32 s14, s11, 0x60
	s_lshl_b32 s11, s14, 7
	s_cmp_gt_i32 s10, 63
	v_add_u32_e32 v4, v20, v18
	v_bitop3_b32 v145, v22, s11, v21 bitop3:0xde
	s_waitcnt vmcnt(6)
	s_cselect_b64 s[10:11], -1, 0
	s_add_i32 s49, s46, -2
	v_add_lshl_u32 v4, v4, v19, 1
	v_mov_b32_e32 v5, v3
	v_add_u32_e32 v2, v17, v2
	s_cmpk_lt_u32 s12, 0x100
	v_lshl_add_u64 v[140:141], s[2:3], 0, v[4:5]
	v_add_lshl_u32 v4, v2, v16, 1
	s_cselect_b64 s[12:13], -1, 0
	v_or_b32_e32 v146, s14, v23
	v_lshl_add_u64 v[142:143], s[2:3], 0, v[4:5]
	s_mov_b32 s50, 0
	v_add_u32_e32 v147, 0, v24
	v_readlane_b32 s53, v254, 29
	v_readlane_b32 s54, v254, 27
	s_barrier
	s_waitcnt vmcnt(0)
	s_mov_b32 s100, 0
	s_branch .LBB0_3491

.LBB0_3497:
	s_andn2_b64 vcc, exec, s[10:11]
	s_cbranch_vccnz .LBB0_3500
	s_add_u32 s26, s26, 0x80
	s_addc_u32 s27, s27, 0
	s_add_u32 s19, s30, 0x100
	s_addc_u32 s20, s31, 0
	s_mov_b32 s21, 0
	s_add_i32 s22, s21, 2
	s_add_u32 s23, s26, 0x80
	s_addc_u32 s28, s27, 0
	s_add_i32 s55, 0, 0x10000
	s_cmp_eq_u32 s49, s21
	s_cselect_b32 s31, s15, s28
	s_cselect_b32 s30, s14, s23
	v_add_u32_e32 v2, s55, v145
	s_cselect_b32 s29, s17, s20
	s_cselect_b32 s28, s16, s19
	s_add_i32 s21, 0, 0x14000
	ds_read_b128 v[148:151], v2
	ds_read_b128 v[152:155], v2 offset:1024
	ds_read_b128 v[156:159], v2 offset:2048
	ds_read_b128 v[160:163], v2 offset:3072
	v_add_u32_e32 v2, s21, v145
	ds_read_b128 v[164:167], v2
	ds_read_b128 v[168:171], v2 offset:1024
	ds_read_b128 v[172:175], v2 offset:2048
	ds_read_b128 v[176:179], v2 offset:3072
	v_lshl_add_u64 v[212:213], s[26:27], 0, v[140:141]
	s_add_i32 m0, s42, 0xc000
	ds_read_b128 v[180:183], v147
	ds_read_b128 v[184:187], v147 offset:1024
	ds_read_b128 v[188:191], v147 offset:2048
	ds_read_b128 v[192:195], v147 offset:3072
	ds_read_b128 v[196:199], v147 offset:4096
	ds_read_b128 v[200:203], v147 offset:5120
	ds_read_b128 v[204:207], v147 offset:6144
	ds_read_b128 v[208:211], v147 offset:7168
	global_load_lds_dwordx4 v[212:213], off
	v_lshl_add_u64 v[212:213], s[26:27], 0, v[142:143]
	s_add_i32 m0, s42, 0xe000
	s_nop 0
	global_load_lds_dwordx4 v[212:213], off
	s_cmp_eq_u32 s100, 0
	s_cbranch_scc1 .Lmy_w20a
	s_waitcnt vmcnt(16)
	s_branch .Lmy_w20b

.Lmy_w20b:
	s_waitcnt lgkmcnt(0)
	s_barrier
	s_setprio 1
	v_mfma_f32_16x16x32_bf16 v[124:127], v[148:151], v[180:183], 0
	v_mfma_f32_16x16x32_bf16 v[128:131], v[156:159], v[180:183], 0
	v_mfma_f32_16x16x32_bf16 v[112:115], v[148:151], v[188:191], 0
	v_mfma_f32_16x16x32_bf16 v[108:111], v[156:159], v[188:191], 0
	v_mfma_f32_16x16x32_bf16 v[96:99], v[148:151], v[196:199], 0
	v_mfma_f32_16x16x32_bf16 v[92:95], v[156:159], v[196:199], 0
	v_mfma_f32_16x16x32_bf16 v[80:83], v[148:151], v[204:207], 0
	v_mfma_f32_16x16x32_bf16 v[76:79], v[156:159], v[204:207], 0
	v_mfma_f32_16x16x32_bf16 v[124:127], v[152:155], v[184:187], v[124:127]
	v_mfma_f32_16x16x32_bf16 v[128:131], v[160:163], v[184:187], v[128:131]
	v_mfma_f32_16x16x32_bf16 v[112:115], v[152:155], v[192:195], v[112:115]
	v_mfma_f32_16x16x32_bf16 v[108:111], v[160:163], v[192:195], v[108:111]
	v_mfma_f32_16x16x32_bf16 v[96:99], v[152:155], v[200:203], v[96:99]
	v_mfma_f32_16x16x32_bf16 v[92:95], v[160:163], v[200:203], v[92:95]
	v_mfma_f32_16x16x32_bf16 v[80:83], v[152:155], v[208:211], v[80:83]
	v_mfma_f32_16x16x32_bf16 v[76:79], v[160:163], v[208:211], v[76:79]
	s_setprio 0
	s_setprio 1
	v_mfma_f32_16x16x32_bf16 v[120:123], v[164:167], v[180:183], 0
	v_mfma_f32_16x16x32_bf16 v[116:119], v[172:175], v[180:183], 0
	v_mfma_f32_16x16x32_bf16 v[104:107], v[164:167], v[188:191], 0
	v_mfma_f32_16x16x32_bf16 v[100:103], v[172:175], v[188:191], 0
	v_mfma_f32_16x16x32_bf16 v[88:91], v[164:167], v[196:199], 0
	v_mfma_f32_16x16x32_bf16 v[84:87], v[172:175], v[196:199], 0
	v_mfma_f32_16x16x32_bf16 v[72:75], v[164:167], v[204:207], 0
	v_mfma_f32_16x16x32_bf16 v[68:71], v[172:175], v[204:207], 0
	v_mfma_f32_16x16x32_bf16 v[120:123], v[168:171], v[184:187], v[120:123]
	v_mfma_f32_16x16x32_bf16 v[116:119], v[176:179], v[184:187], v[116:119]
	v_mfma_f32_16x16x32_bf16 v[104:107], v[168:171], v[192:195], v[104:107]
	v_mfma_f32_16x16x32_bf16 v[100:103], v[176:179], v[192:195], v[100:103]
	v_mfma_f32_16x16x32_bf16 v[88:91], v[168:171], v[200:203], v[88:91]
	v_mfma_f32_16x16x32_bf16 v[84:87], v[176:179], v[200:203], v[84:87]
	v_mfma_f32_16x16x32_bf16 v[72:75], v[168:171], v[208:211], v[72:75]
	v_mfma_f32_16x16x32_bf16 v[68:71], v[176:179], v[208:211], v[68:71]
	s_barrier
	s_setprio 0
	s_add_i32 s23, s55, s41
	v_lshl_add_u64 v[212:213], s[28:29], 0, v[136:137]
	s_mov_b32 m0, s23
	ds_read_b128 v[180:183], v147 offset:16384
	ds_read_b128 v[184:187], v147 offset:17408
	ds_read_b128 v[188:191], v147 offset:18432
	ds_read_b128 v[192:195], v147 offset:19456
	ds_read_b128 v[196:199], v147 offset:20480
	ds_read_b128 v[200:203], v147 offset:21504
	ds_read_b128 v[204:207], v147 offset:22528
	ds_read_b128 v[208:211], v147 offset:23552
	global_load_lds_dwordx4 v[212:213], off
	s_add_i32 m0, s23, 0x2000
	v_lshl_add_u64 v[214:215], s[28:29], 0, v[132:133]
	s_add_u32 s28, s28, s2
	s_addc_u32 s29, s29, s3
	s_add_i32 s21, s21, s41
	global_load_lds_dwordx4 v[214:215], off
	v_lshl_add_u64 v[218:219], s[28:29], 0, v[136:137]
	s_mov_b32 m0, s21
	v_lshl_add_u64 v[220:221], s[28:29], 0, v[132:133]
	global_load_lds_dwordx4 v[218:219], off
	s_add_i32 m0, s21, 0x2000
	v_lshl_add_u64 v[222:223], s[30:31], 0, v[138:139]
	global_load_lds_dwordx4 v[220:221], off
	s_mov_b32 m0, s42
	v_lshl_add_u64 v[224:225], s[30:31], 0, v[134:135]
	global_load_lds_dwordx4 v[222:223], off
	s_mov_b32 m0, s43
	s_nop 0
	global_load_lds_dwordx4 v[224:225], off
	s_cmp_eq_u32 s100, 0
	s_cbranch_scc1 .Lmy_w21a
	s_waitcnt vmcnt(16)
	s_branch .Lmy_w21b

.Lmy_w21b:
	s_mov_b32 s100, 1
	s_waitcnt lgkmcnt(0)
	s_barrier
	s_setprio 1
	v_mfma_f32_16x16x32_bf16 v[64:67], v[148:151], v[180:183], 0
	v_mfma_f32_16x16x32_bf16 v[60:63], v[156:159], v[180:183], 0
	v_mfma_f32_16x16x32_bf16 v[48:51], v[148:151], v[188:191], 0
	v_mfma_f32_16x16x32_bf16 v[44:47], v[156:159], v[188:191], 0
	v_mfma_f32_16x16x32_bf16 v[32:35], v[148:151], v[196:199], 0
	v_mfma_f32_16x16x32_bf16 v[28:31], v[156:159], v[196:199], 0
	v_mfma_f32_16x16x32_bf16 v[16:19], v[148:151], v[204:207], 0
	v_mfma_f32_16x16x32_bf16 v[12:15], v[156:159], v[204:207], 0
	v_mfma_f32_16x16x32_bf16 v[64:67], v[152:155], v[184:187], v[64:67]
	v_mfma_f32_16x16x32_bf16 v[60:63], v[160:163], v[184:187], v[60:63]
	v_mfma_f32_16x16x32_bf16 v[48:51], v[152:155], v[192:195], v[48:51]
	v_mfma_f32_16x16x32_bf16 v[44:47], v[160:163], v[192:195], v[44:47]
	v_mfma_f32_16x16x32_bf16 v[32:35], v[152:155], v[200:203], v[32:35]
	v_mfma_f32_16x16x32_bf16 v[28:31], v[160:163], v[200:203], v[28:31]
	v_mfma_f32_16x16x32_bf16 v[16:19], v[152:155], v[208:211], v[16:19]
	v_mfma_f32_16x16x32_bf16 v[12:15], v[160:163], v[208:211], v[12:15]
	s_setprio 0
	s_setprio 1
	v_mfma_f32_16x16x32_bf16 v[56:59], v[164:167], v[180:183], 0
	v_mfma_f32_16x16x32_bf16 v[52:55], v[172:175], v[180:183], 0
	v_mfma_f32_16x16x32_bf16 v[40:43], v[164:167], v[188:191], 0
	v_mfma_f32_16x16x32_bf16 v[36:39], v[172:175], v[188:191], 0
	v_mfma_f32_16x16x32_bf16 v[24:27], v[164:167], v[196:199], 0
	v_mfma_f32_16x16x32_bf16 v[20:23], v[172:175], v[196:199], 0
	v_mfma_f32_16x16x32_bf16 v[8:11], v[164:167], v[204:207], 0
	v_mfma_f32_16x16x32_bf16 v[4:7], v[172:175], v[204:207], 0
	v_mfma_f32_16x16x32_bf16 v[56:59], v[168:171], v[184:187], v[56:59]
	v_mfma_f32_16x16x32_bf16 v[52:55], v[176:179], v[184:187], v[52:55]
	v_mfma_f32_16x16x32_bf16 v[40:43], v[168:171], v[192:195], v[40:43]
	v_mfma_f32_16x16x32_bf16 v[36:39], v[176:179], v[192:195], v[36:39]
	v_mfma_f32_16x16x32_bf16 v[24:27], v[168:171], v[200:203], v[24:27]
	v_mfma_f32_16x16x32_bf16 v[20:23], v[176:179], v[200:203], v[20:23]
	v_mfma_f32_16x16x32_bf16 v[8:11], v[168:171], v[208:211], v[8:11]
	v_mfma_f32_16x16x32_bf16 v[4:7], v[176:179], v[208:211], v[4:7]
	s_barrier
	s_setprio 0
	s_add_i32 s21, 0, 0x18000
	v_add_u32_e32 v2, s21, v145
	s_add_i32 s23, 0, 0x1c000
	ds_read_b128 v[148:151], v2
	ds_read_b128 v[152:155], v2 offset:1024
	ds_read_b128 v[156:159], v2 offset:2048
	ds_read_b128 v[160:163], v2 offset:3072
	v_add_u32_e32 v2, s23, v145
	ds_read_b128 v[164:167], v2
	ds_read_b128 v[168:171], v2 offset:1024
	ds_read_b128 v[172:175], v2 offset:2048
	ds_read_b128 v[176:179], v2 offset:3072
	s_add_u32 s28, s30, s2
	s_addc_u32 s29, s31, s3
	s_mov_b32 m0, s44
	v_lshl_add_u64 v[226:227], s[28:29], 0, v[138:139]
	ds_read_b128 v[180:183], v147 offset:32768
	ds_read_b128 v[184:187], v147 offset:33792
	ds_read_b128 v[188:191], v147 offset:34816
	ds_read_b128 v[192:195], v147 offset:35840
	ds_read_b128 v[196:199], v147 offset:36864
	ds_read_b128 v[200:203], v147 offset:37888
	ds_read_b128 v[204:207], v147 offset:38912
	ds_read_b128 v[208:211], v147 offset:39936
	global_load_lds_dwordx4 v[226:227], off
	v_lshl_add_u64 v[226:227], s[28:29], 0, v[134:135]
	s_mov_b32 m0, s45
	s_nop 0
	global_load_lds_dwordx4 v[226:227], off
	s_waitcnt vmcnt(8)
	s_waitcnt lgkmcnt(0)
	s_barrier
	s_setprio 1
	v_mfma_f32_16x16x32_bf16 v[124:127], v[148:151], v[180:183], v[124:127]
	v_mfma_f32_16x16x32_bf16 v[128:131], v[156:159], v[180:183], v[128:131]
	v_mfma_f32_16x16x32_bf16 v[112:115], v[148:151], v[188:191], v[112:115]
	v_mfma_f32_16x16x32_bf16 v[108:111], v[156:159], v[188:191], v[108:111]
	v_mfma_f32_16x16x32_bf16 v[96:99], v[148:151], v[196:199], v[96:99]
	v_mfma_f32_16x16x32_bf16 v[92:95], v[156:159], v[196:199], v[92:95]
	v_mfma_f32_16x16x32_bf16 v[80:83], v[148:151], v[204:207], v[80:83]
	v_mfma_f32_16x16x32_bf16 v[76:79], v[156:159], v[204:207], v[76:79]
	v_mfma_f32_16x16x32_bf16 v[124:127], v[152:155], v[184:187], v[124:127]
	v_mfma_f32_16x16x32_bf16 v[128:131], v[160:163], v[184:187], v[128:131]
	v_mfma_f32_16x16x32_bf16 v[112:115], v[152:155], v[192:195], v[112:115]
	v_mfma_f32_16x16x32_bf16 v[108:111], v[160:163], v[192:195], v[108:111]
	v_mfma_f32_16x16x32_bf16 v[96:99], v[152:155], v[200:203], v[96:99]
	v_mfma_f32_16x16x32_bf16 v[92:95], v[160:163], v[200:203], v[92:95]
	v_mfma_f32_16x16x32_bf16 v[80:83], v[152:155], v[208:211], v[80:83]
	v_mfma_f32_16x16x32_bf16 v[76:79], v[160:163], v[208:211], v[76:79]
	s_setprio 0
	s_setprio 1
	v_mfma_f32_16x16x32_bf16 v[120:123], v[164:167], v[180:183], v[120:123]
	v_mfma_f32_16x16x32_bf16 v[116:119], v[172:175], v[180:183], v[116:119]
	v_mfma_f32_16x16x32_bf16 v[104:107], v[164:167], v[188:191], v[104:107]
	v_mfma_f32_16x16x32_bf16 v[100:103], v[172:175], v[188:191], v[100:103]
	v_mfma_f32_16x16x32_bf16 v[88:91], v[164:167], v[196:199], v[88:91]
	v_mfma_f32_16x16x32_bf16 v[84:87], v[172:175], v[196:199], v[84:87]
	v_mfma_f32_16x16x32_bf16 v[72:75], v[164:167], v[204:207], v[72:75]
	v_mfma_f32_16x16x32_bf16 v[68:71], v[172:175], v[204:207], v[68:71]
	v_mfma_f32_16x16x32_bf16 v[120:123], v[168:171], v[184:187], v[120:123]
	v_mfma_f32_16x16x32_bf16 v[116:119], v[176:179], v[184:187], v[116:119]
	v_mfma_f32_16x16x32_bf16 v[104:107], v[168:171], v[192:195], v[104:107]
	v_mfma_f32_16x16x32_bf16 v[100:103], v[176:179], v[192:195], v[100:103]
	v_mfma_f32_16x16x32_bf16 v[88:91], v[168:171], v[200:203], v[88:91]
	v_mfma_f32_16x16x32_bf16 v[84:87], v[176:179], v[200:203], v[84:87]
	v_mfma_f32_16x16x32_bf16 v[72:75], v[168:171], v[208:211], v[72:75]
	v_mfma_f32_16x16x32_bf16 v[68:71], v[176:179], v[208:211], v[68:71]
	s_barrier
	s_setprio 0
	s_add_i32 s21, s21, s41
	v_lshl_add_u64 v[212:213], v[212:213], 0, s[24:25]
	s_mov_b32 m0, s21
	ds_read_b128 v[180:183], v147 offset:49152
	ds_read_b128 v[184:187], v147 offset:50176
	ds_read_b128 v[188:191], v147 offset:51200
	ds_read_b128 v[192:195], v147 offset:52224
	ds_read_b128 v[196:199], v147 offset:53248
	ds_read_b128 v[200:203], v147 offset:54272
	ds_read_b128 v[204:207], v147 offset:55296
	ds_read_b128 v[208:211], v147 offset:56320
	global_load_lds_dwordx4 v[212:213], off
	v_lshl_add_u64 v[212:213], v[214:215], 0, s[24:25]
	s_add_i32 m0, s21, 0x2000
	s_add_i32 s21, s23, s41
	global_load_lds_dwordx4 v[212:213], off
	v_lshl_add_u64 v[212:213], v[218:219], 0, s[24:25]
	s_mov_b32 m0, s21
	s_nop 0
	global_load_lds_dwordx4 v[212:213], off
	v_lshl_add_u64 v[212:213], v[220:221], 0, s[24:25]
	s_add_i32 m0, s21, 0x2000
	s_nop 0
	global_load_lds_dwordx4 v[212:213], off
	v_lshl_add_u64 v[212:213], v[222:223], 0, s[24:25]
	s_mov_b32 m0, s47
	s_nop 0
	global_load_lds_dwordx4 v[212:213], off
	v_lshl_add_u64 v[212:213], v[224:225], 0, s[24:25]
	s_mov_b32 m0, s48
	s_nop 0
	global_load_lds_dwordx4 v[212:213], off
	s_waitcnt vmcnt(8)
	s_waitcnt lgkmcnt(0)
	s_barrier
	s_setprio 1
	v_mfma_f32_16x16x32_bf16 v[64:67], v[148:151], v[180:183], v[64:67]
	v_mfma_f32_16x16x32_bf16 v[60:63], v[156:159], v[180:183], v[60:63]
	v_mfma_f32_16x16x32_bf16 v[48:51], v[148:151], v[188:191], v[48:51]
	v_mfma_f32_16x16x32_bf16 v[44:47], v[156:159], v[188:191], v[44:47]
	v_mfma_f32_16x16x32_bf16 v[32:35], v[148:151], v[196:199], v[32:35]
	v_mfma_f32_16x16x32_bf16 v[28:31], v[156:159], v[196:199], v[28:31]
	v_mfma_f32_16x16x32_bf16 v[16:19], v[148:151], v[204:207], v[16:19]
	v_mfma_f32_16x16x32_bf16 v[12:15], v[156:159], v[204:207], v[12:15]
	v_mfma_f32_16x16x32_bf16 v[64:67], v[152:155], v[184:187], v[64:67]
	v_mfma_f32_16x16x32_bf16 v[60:63], v[160:163], v[184:187], v[60:63]
	v_mfma_f32_16x16x32_bf16 v[48:51], v[152:155], v[192:195], v[48:51]
	v_mfma_f32_16x16x32_bf16 v[44:47], v[160:163], v[192:195], v[44:47]
	v_mfma_f32_16x16x32_bf16 v[32:35], v[152:155], v[200:203], v[32:35]
	v_mfma_f32_16x16x32_bf16 v[28:31], v[160:163], v[200:203], v[28:31]
	v_mfma_f32_16x16x32_bf16 v[16:19], v[152:155], v[208:211], v[16:19]
	v_mfma_f32_16x16x32_bf16 v[12:15], v[160:163], v[208:211], v[12:15]
	s_setprio 0
	s_setprio 1
	v_mfma_f32_16x16x32_bf16 v[56:59], v[164:167], v[180:183], v[56:59]
	v_mfma_f32_16x16x32_bf16 v[52:55], v[172:175], v[180:183], v[52:55]
	v_mfma_f32_16x16x32_bf16 v[40:43], v[164:167], v[188:191], v[40:43]
	v_mfma_f32_16x16x32_bf16 v[36:39], v[172:175], v[188:191], v[36:39]
	v_mfma_f32_16x16x32_bf16 v[24:27], v[164:167], v[196:199], v[24:27]
	v_mfma_f32_16x16x32_bf16 v[20:23], v[172:175], v[196:199], v[20:23]
	v_mfma_f32_16x16x32_bf16 v[8:11], v[164:167], v[204:207], v[8:11]
	v_mfma_f32_16x16x32_bf16 v[4:7], v[172:175], v[204:207], v[4:7]
	v_mfma_f32_16x16x32_bf16 v[56:59], v[168:171], v[184:187], v[56:59]
	v_mfma_f32_16x16x32_bf16 v[52:55], v[176:179], v[184:187], v[52:55]
	v_mfma_f32_16x16x32_bf16 v[40:43], v[168:171], v[192:195], v[40:43]
	v_mfma_f32_16x16x32_bf16 v[36:39], v[176:179], v[192:195], v[36:39]
	v_mfma_f32_16x16x32_bf16 v[24:27], v[168:171], v[200:203], v[24:27]
	v_mfma_f32_16x16x32_bf16 v[20:23], v[176:179], v[200:203], v[20:23]
	v_mfma_f32_16x16x32_bf16 v[8:11], v[168:171], v[208:211], v[8:11]
	v_mfma_f32_16x16x32_bf16 v[4:7], v[176:179], v[208:211], v[4:7]
	s_barrier
	s_setprio 0
	s_add_u32 s26, s26, 0x100
	s_addc_u32 s27, s27, 0
	s_add_u32 s19, s19, 0x100
	s_addc_u32 s20, s20, 0
	s_cmp_ge_i32 s22, s46
	s_mov_b32 s21, s22
	s_cbranch_scc1 .LBB0_3500
